# P4 output stores sc0 sc1 instead of sc1
# speedup vs baseline: 1.0162x; 1.0162x over previous
.LBB5_34:
	s_lshl_b32 s1, s3, 6
	v_lshlrev_b32_e32 v0, 2, v195
	v_mov_b32_e32 v24, 0x3fffffcc
	v_lshl_or_b32 v0, s35, 5, v0
	s_add_i32 s0, 0, 0x20000
	v_bitop3_b32 v24, s1, v24, v194 bitop3:0xc8
	v_or_b32_e32 v28, s24, v0
	v_lshlrev_b32_e32 v0, 2, v0
	v_add_u32_e32 v24, s0, v24
	s_nop 15
	s_nop 15
	v_add_u32_e32 v34, s0, v0
	v_add_u32_e32 v0, 0, v0
	v_add_u32_e32 v46, 0x800, v24
	v_or_b32_e32 v44, s1, v194
	v_add_u32_e32 v35, 0x20400, v0
	ds_read_b128 v[16:19], v34
	ds_read_b128 v[8:11], v34 offset:64
	ds_read_b128 v[20:23], v35
	ds_read_b128 v[12:15], v35 offset:64
	ds_read_b128 v[4:7], v34 offset:512
	ds_read_b128 v[0:3], v35 offset:512
	ds_read2_b32 v[40:41], v46 offset1:4
	v_add_u32_e32 v38, s6, v44
	v_ashrrev_i32_e32 v39, 31, v38
	v_ashrrev_i32_e32 v29, 31, v28
	v_lshlrev_b64 v[30:31], 13, v[38:39]
	s_waitcnt lgkmcnt(6)
	v_pk_fma_f32 v[26:27], s[2:3], v[190:191], v[18:19] op_sel_hi:[0,1,1]
	v_pk_fma_f32 v[24:25], s[2:3], v[188:189], v[16:17] op_sel_hi:[0,1,1]
	v_lshl_add_u64 v[30:31], s[4:5], 0, v[30:31]
	v_lshlrev_b64 v[42:43], 2, v[28:29]
	s_waitcnt lgkmcnt(0)
	v_pk_fma_f32 v[24:25], v[20:21], v[40:41], v[24:25] op_sel_hi:[1,0,1]
	v_pk_fma_f32 v[26:27], v[22:23], v[40:41], v[26:27] op_sel_hi:[1,0,1]
	v_lshl_add_u64 v[32:33], v[30:31], 0, v[42:43]
	global_store_dwordx4 v[32:33], v[24:27], off sc0 sc1
	v_pk_fma_f32 v[36:37], s[2:3], v[182:183], v[6:7] op_sel_hi:[0,1,1]
	v_pk_fma_f32 v[36:37], v[2:3], v[40:41], v[36:37] op_sel_hi:[1,0,1]
	v_pk_fma_f32 v[24:25], s[2:3], v[186:187], v[10:11] op_sel_hi:[0,1,1]
	v_pk_fma_f32 v[26:27], s[2:3], v[184:185], v[8:9] op_sel_hi:[0,1,1]
	v_pk_fma_f32 v[28:29], v[12:13], v[40:41], v[26:27] op_sel_hi:[1,0,1]
	v_pk_fma_f32 v[30:31], v[14:15], v[40:41], v[24:25] op_sel_hi:[1,0,1]
	ds_read_b128 v[24:27], v34 offset:576
	global_store_dwordx4 v[32:33], v[28:31], off offset:64 sc0 sc1
	ds_read_b128 v[28:31], v35 offset:576
	v_pk_fma_f32 v[34:35], s[2:3], v[180:181], v[4:5] op_sel_hi:[0,1,1]
	v_pk_fma_f32 v[34:35], v[0:1], v[40:41], v[34:35] op_sel_hi:[1,0,1]
	global_store_dwordx4 v[32:33], v[34:37], off offset:512 sc0 sc1
	v_add_u32_e32 v48, 0x80, v44
	v_add_u32_e32 v49, 0x90, v44
	s_waitcnt lgkmcnt(1)
	v_pk_fma_f32 v[36:37], s[2:3], v[174:175], v[26:27] op_sel_hi:[0,1,1]
	v_pk_fma_f32 v[34:35], s[2:3], v[172:173], v[24:25] op_sel_hi:[0,1,1]
	s_waitcnt lgkmcnt(0)
	v_pk_fma_f32 v[34:35], v[28:29], v[40:41], v[34:35] op_sel_hi:[1,0,1]
	v_pk_fma_f32 v[36:37], v[30:31], v[40:41], v[36:37] op_sel_hi:[1,0,1]
	global_store_dwordx4 v[32:33], v[34:37], off offset:576 sc0 sc1
	v_add_u32_e32 v50, 0xa0, v44
	v_add_u32_e32 v51, 0xb0, v44
	v_or_b32_e32 v34, 16, v38
	v_ashrrev_i32_e32 v35, 31, v34
	v_lshlrev_b64 v[34:35], 13, v[34:35]
	v_lshl_add_u64 v[34:35], s[4:5], 0, v[34:35]
	v_lshl_add_u64 v[44:45], v[34:35], 0, v[42:43]
	v_pk_fma_f32 v[36:37], s[2:3], v[178:179], v[18:19] op_sel_hi:[0,1,1]
	v_pk_fma_f32 v[34:35], s[2:3], v[176:177], v[16:17] op_sel_hi:[0,1,1]
	v_mov_b32_e32 v40, v41
	v_pk_fma_f32 v[34:35], v[20:21], v[40:41], v[34:35] op_sel_hi:[1,0,1]
	v_pk_fma_f32 v[36:37], v[22:23], v[40:41], v[36:37] op_sel_hi:[1,0,1]
	global_store_dwordx4 v[44:45], v[34:37], off sc0 sc1
	s_cmpk_lt_u32 s28, 0x100
	s_nop 0
	v_pk_fma_f32 v[36:37], s[2:3], v[170:171], v[10:11] op_sel_hi:[0,1,1]
	v_pk_fma_f32 v[34:35], s[2:3], v[168:169], v[8:9] op_sel_hi:[0,1,1]
	v_pk_fma_f32 v[34:35], v[12:13], v[40:41], v[34:35] op_sel_hi:[1,0,1]
	v_pk_fma_f32 v[36:37], v[14:15], v[40:41], v[36:37] op_sel_hi:[1,0,1]
	global_store_dwordx4 v[44:45], v[34:37], off offset:64 sc0 sc1
	s_nop 1
	v_pk_fma_f32 v[36:37], s[2:3], v[166:167], v[6:7] op_sel_hi:[0,1,1]
	v_pk_fma_f32 v[34:35], s[2:3], v[164:165], v[4:5] op_sel_hi:[0,1,1]
	v_pk_fma_f32 v[34:35], v[0:1], v[40:41], v[34:35] op_sel_hi:[1,0,1]
	v_pk_fma_f32 v[36:37], v[2:3], v[40:41], v[36:37] op_sel_hi:[1,0,1]
	global_store_dwordx4 v[44:45], v[34:37], off offset:512 sc0 sc1
	s_nop 1
	v_pk_fma_f32 v[36:37], s[2:3], v[158:159], v[26:27] op_sel_hi:[0,1,1]
	v_pk_fma_f32 v[34:35], s[2:3], v[156:157], v[24:25] op_sel_hi:[0,1,1]
	v_pk_fma_f32 v[34:35], v[28:29], v[40:41], v[34:35] op_sel_hi:[1,0,1]
	v_pk_fma_f32 v[36:37], v[30:31], v[40:41], v[36:37] op_sel_hi:[1,0,1]
	global_store_dwordx4 v[44:45], v[34:37], off offset:576 sc0 sc1
	ds_read2_b32 v[40:41], v46 offset0:8 offset1:12
	v_pk_fma_f32 v[46:47], s[2:3], v[160:161], v[16:17] op_sel_hi:[0,1,1]
	v_or_b32_e32 v34, 32, v38
	v_ashrrev_i32_e32 v35, 31, v34
	v_lshlrev_b64 v[34:35], 13, v[34:35]
	v_lshl_add_u64 v[34:35], s[4:5], 0, v[34:35]
	v_lshl_add_u64 v[44:45], v[34:35], 0, v[42:43]
	v_pk_fma_f32 v[34:35], s[2:3], v[162:163], v[18:19] op_sel_hi:[0,1,1]
	s_waitcnt lgkmcnt(0)
	v_pk_fma_f32 v[36:37], v[22:23], v[40:41], v[34:35] op_sel_hi:[1,0,1]
	v_pk_fma_f32 v[34:35], v[20:21], v[40:41], v[46:47] op_sel_hi:[1,0,1]
	global_store_dwordx4 v[44:45], v[34:37], off sc0 sc1
	v_pk_fma_f32 v[46:47], s[2:3], v[152:153], v[8:9] op_sel_hi:[0,1,1]
	s_nop 0
	v_pk_fma_f32 v[34:35], s[2:3], v[154:155], v[10:11] op_sel_hi:[0,1,1]
	v_pk_fma_f32 v[36:37], v[14:15], v[40:41], v[34:35] op_sel_hi:[1,0,1]
	v_pk_fma_f32 v[34:35], v[12:13], v[40:41], v[46:47] op_sel_hi:[1,0,1]
	global_store_dwordx4 v[44:45], v[34:37], off offset:64 sc0 sc1
	v_pk_fma_f32 v[46:47], s[2:3], v[148:149], v[4:5] op_sel_hi:[0,1,1]
	s_nop 0
	v_pk_fma_f32 v[34:35], s[2:3], v[150:151], v[6:7] op_sel_hi:[0,1,1]
	v_pk_fma_f32 v[36:37], v[2:3], v[40:41], v[34:35] op_sel_hi:[1,0,1]
	v_pk_fma_f32 v[34:35], v[0:1], v[40:41], v[46:47] op_sel_hi:[1,0,1]
	global_store_dwordx4 v[44:45], v[34:37], off offset:512 sc0 sc1
	v_pk_fma_f32 v[46:47], s[2:3], v[140:141], v[24:25] op_sel_hi:[0,1,1]
	s_nop 0
	v_pk_fma_f32 v[34:35], s[2:3], v[142:143], v[26:27] op_sel_hi:[0,1,1]
	v_pk_fma_f32 v[36:37], v[30:31], v[40:41], v[34:35] op_sel_hi:[1,0,1]
	v_pk_fma_f32 v[34:35], v[28:29], v[40:41], v[46:47] op_sel_hi:[1,0,1]
	global_store_dwordx4 v[44:45], v[34:37], off offset:576 sc0 sc1
	v_mov_b32_e32 v40, v41
	s_nop 0
	v_or_b32_e32 v34, 48, v38
	v_ashrrev_i32_e32 v35, 31, v34
	v_lshlrev_b64 v[34:35], 13, v[34:35]
	v_lshl_add_u64 v[34:35], s[4:5], 0, v[34:35]
	v_lshl_add_u64 v[38:39], v[34:35], 0, v[42:43]
	v_pk_fma_f32 v[34:35], s[2:3], v[146:147], v[18:19] op_sel_hi:[0,1,1]
	v_pk_fma_f32 v[42:43], s[2:3], v[144:145], v[16:17] op_sel_hi:[0,1,1]
	v_pk_fma_f32 v[36:37], v[22:23], v[40:41], v[34:35] op_sel_hi:[1,0,1]
	v_pk_fma_f32 v[34:35], v[20:21], v[40:41], v[42:43] op_sel_hi:[1,0,1]
	global_store_dwordx4 v[38:39], v[34:37], off sc0 sc1
	v_pk_fma_f32 v[42:43], s[2:3], v[136:137], v[8:9] op_sel_hi:[0,1,1]
	s_mov_b64 s[4:5], 0x100000
	v_pk_fma_f32 v[34:35], s[2:3], v[138:139], v[10:11] op_sel_hi:[0,1,1]
	v_pk_fma_f32 v[36:37], v[14:15], v[40:41], v[34:35] op_sel_hi:[1,0,1]
	v_pk_fma_f32 v[34:35], v[12:13], v[40:41], v[42:43] op_sel_hi:[1,0,1]
	global_store_dwordx4 v[38:39], v[34:37], off offset:64 sc0 sc1
	v_pk_fma_f32 v[42:43], s[2:3], v[132:133], v[4:5] op_sel_hi:[0,1,1]
	s_nop 0
	v_pk_fma_f32 v[34:35], s[2:3], v[134:135], v[6:7] op_sel_hi:[0,1,1]
	v_pk_fma_f32 v[36:37], v[2:3], v[40:41], v[34:35] op_sel_hi:[1,0,1]
	v_pk_fma_f32 v[34:35], v[0:1], v[40:41], v[42:43] op_sel_hi:[1,0,1]
	global_store_dwordx4 v[38:39], v[34:37], off offset:512 sc0 sc1
	v_pk_fma_f32 v[42:43], s[2:3], v[128:129], v[24:25] op_sel_hi:[0,1,1]
	s_nop 0
	v_pk_fma_f32 v[34:35], s[2:3], v[130:131], v[26:27] op_sel_hi:[0,1,1]
	v_pk_fma_f32 v[36:37], v[30:31], v[40:41], v[34:35] op_sel_hi:[1,0,1]
	v_pk_fma_f32 v[34:35], v[28:29], v[40:41], v[42:43] op_sel_hi:[1,0,1]
	global_store_dwordx4 v[38:39], v[34:37], off offset:576 sc0 sc1
	v_and_b32_e32 v39, 0x7ffffffc, v51
	v_pk_fma_f32 v[42:43], s[2:3], v[124:125], v[16:17] op_sel_hi:[0,1,1]
	v_and_b32_e32 v34, 0x7fffffcc, v48
	v_add_u32_e32 v34, s0, v34
	ds_read_b32 v38, v34 offset:2048
	v_and_b32_e32 v36, 0x7fffffdc, v49
	v_and_b32_e32 v37, 0x7fffffec, v50
	v_pk_fma_f32 v[34:35], s[2:3], v[126:127], v[18:19] op_sel_hi:[0,1,1]
	v_add_u32_e32 v36, s0, v36
	v_add_u32_e32 v37, s0, v37
	v_add_u32_e32 v39, s0, v39
	s_mov_b32 s0, 0x100000
	ds_read_b32 v44, v36 offset:2048
	ds_read_b32 v46, v37 offset:2048
	ds_read_b32 v48, v39 offset:2048
	s_waitcnt lgkmcnt(3)
	v_pk_fma_f32 v[36:37], v[22:23], v[38:39], v[34:35] op_sel_hi:[1,0,1]
	v_pk_fma_f32 v[34:35], v[20:21], v[38:39], v[42:43] op_sel_hi:[1,0,1]
	v_add_co_u32_e32 v42, vcc, s0, v32
	v_lshl_add_u64 v[40:41], v[32:33], 0, s[4:5]
	s_nop 0
	v_addc_co_u32_e32 v43, vcc, 0, v33, vcc
	global_store_dwordx4 v[42:43], v[34:37], off sc0 sc1
	v_pk_fma_f32 v[42:43], s[2:3], v[120:121], v[8:9] op_sel_hi:[0,1,1]
	s_mov_b64 s[0:1], 0x120000
	v_pk_fma_f32 v[34:35], s[2:3], v[122:123], v[10:11] op_sel_hi:[0,1,1]
	v_pk_fma_f32 v[36:37], v[14:15], v[38:39], v[34:35] op_sel_hi:[1,0,1]
	v_pk_fma_f32 v[34:35], v[12:13], v[38:39], v[42:43] op_sel_hi:[1,0,1]
	global_store_dwordx4 v[40:41], v[34:37], off offset:64 sc0 sc1
	v_pk_fma_f32 v[42:43], s[2:3], v[108:109], v[4:5] op_sel_hi:[0,1,1]
	s_nop 0
	v_pk_fma_f32 v[34:35], s[2:3], v[110:111], v[6:7] op_sel_hi:[0,1,1]
	v_pk_fma_f32 v[36:37], v[2:3], v[38:39], v[34:35] op_sel_hi:[1,0,1]
	v_pk_fma_f32 v[34:35], v[0:1], v[38:39], v[42:43] op_sel_hi:[1,0,1]
	global_store_dwordx4 v[40:41], v[34:37], off offset:512 sc0 sc1
	v_pk_fma_f32 v[42:43], s[2:3], v[104:105], v[24:25] op_sel_hi:[0,1,1]
	s_nop 0
	v_pk_fma_f32 v[34:35], s[2:3], v[106:107], v[26:27] op_sel_hi:[0,1,1]
	v_pk_fma_f32 v[36:37], v[30:31], v[38:39], v[34:35] op_sel_hi:[1,0,1]
	v_pk_fma_f32 v[34:35], v[28:29], v[38:39], v[42:43] op_sel_hi:[1,0,1]
	global_store_dwordx4 v[40:41], v[34:37], off offset:576 sc0 sc1
	v_lshl_add_u64 v[38:39], v[32:33], 0, s[0:1]
	v_pk_fma_f32 v[40:41], s[2:3], v[116:117], v[16:17] op_sel_hi:[0,1,1]
	v_pk_fma_f32 v[34:35], s[2:3], v[118:119], v[18:19] op_sel_hi:[0,1,1]
	s_mov_b32 s0, 0x120000
	s_waitcnt lgkmcnt(2)
	v_pk_fma_f32 v[36:37], v[22:23], v[44:45], v[34:35] op_sel_hi:[1,0,1]
	v_pk_fma_f32 v[34:35], v[20:21], v[44:45], v[40:41] op_sel_hi:[1,0,1]
	v_add_co_u32_e32 v40, vcc, s0, v32
	s_mov_b64 s[0:1], 0x140000
	s_nop 0
	v_addc_co_u32_e32 v41, vcc, 0, v33, vcc
	global_store_dwordx4 v[40:41], v[34:37], off sc0 sc1
	v_pk_fma_f32 v[40:41], s[2:3], v[112:113], v[8:9] op_sel_hi:[0,1,1]
	s_nop 0
	v_pk_fma_f32 v[34:35], s[2:3], v[114:115], v[10:11] op_sel_hi:[0,1,1]
	v_pk_fma_f32 v[36:37], v[14:15], v[44:45], v[34:35] op_sel_hi:[1,0,1]
	v_pk_fma_f32 v[34:35], v[12:13], v[44:45], v[40:41] op_sel_hi:[1,0,1]
	global_store_dwordx4 v[38:39], v[34:37], off offset:64 sc0 sc1
	v_pk_fma_f32 v[40:41], s[2:3], v[92:93], v[4:5] op_sel_hi:[0,1,1]
	s_nop 0
	v_pk_fma_f32 v[34:35], s[2:3], v[94:95], v[6:7] op_sel_hi:[0,1,1]
	v_pk_fma_f32 v[36:37], v[2:3], v[44:45], v[34:35] op_sel_hi:[1,0,1]
	v_pk_fma_f32 v[34:35], v[0:1], v[44:45], v[40:41] op_sel_hi:[1,0,1]
	global_store_dwordx4 v[38:39], v[34:37], off offset:512 sc0 sc1
	v_pk_fma_f32 v[40:41], s[2:3], v[88:89], v[24:25] op_sel_hi:[0,1,1]
	s_nop 0
	v_pk_fma_f32 v[34:35], s[2:3], v[90:91], v[26:27] op_sel_hi:[0,1,1]
	v_pk_fma_f32 v[36:37], v[30:31], v[44:45], v[34:35] op_sel_hi:[1,0,1]
	v_pk_fma_f32 v[34:35], v[28:29], v[44:45], v[40:41] op_sel_hi:[1,0,1]
	global_store_dwordx4 v[38:39], v[34:37], off offset:576 sc0 sc1
	v_lshl_add_u64 v[38:39], v[32:33], 0, s[0:1]
	v_pk_fma_f32 v[40:41], s[2:3], v[100:101], v[16:17] op_sel_hi:[0,1,1]
	v_pk_fma_f32 v[34:35], s[2:3], v[102:103], v[18:19] op_sel_hi:[0,1,1]
	s_mov_b32 s0, 0x140000
	s_waitcnt lgkmcnt(1)
	v_pk_fma_f32 v[36:37], v[22:23], v[46:47], v[34:35] op_sel_hi:[1,0,1]
	v_pk_fma_f32 v[34:35], v[20:21], v[46:47], v[40:41] op_sel_hi:[1,0,1]
	v_add_co_u32_e32 v40, vcc, s0, v32
	s_mov_b64 s[0:1], 0x160000
	s_nop 0
	v_addc_co_u32_e32 v41, vcc, 0, v33, vcc
	global_store_dwordx4 v[40:41], v[34:37], off sc0 sc1
	v_pk_fma_f32 v[40:41], s[2:3], v[96:97], v[8:9] op_sel_hi:[0,1,1]
	v_pk_fma_f32 v[16:17], s[2:3], v[84:85], v[16:17] op_sel_hi:[0,1,1]
	v_pk_fma_f32 v[34:35], s[2:3], v[98:99], v[10:11] op_sel_hi:[0,1,1]
	v_pk_fma_f32 v[36:37], v[14:15], v[46:47], v[34:35] op_sel_hi:[1,0,1]
	v_pk_fma_f32 v[34:35], v[12:13], v[46:47], v[40:41] op_sel_hi:[1,0,1]
	global_store_dwordx4 v[38:39], v[34:37], off offset:64 sc0 sc1
	v_pk_fma_f32 v[40:41], s[2:3], v[80:81], v[4:5] op_sel_hi:[0,1,1]
	v_pk_fma_f32 v[4:5], s[2:3], v[68:69], v[4:5] op_sel_hi:[0,1,1]
	v_pk_fma_f32 v[34:35], s[2:3], v[82:83], v[6:7] op_sel_hi:[0,1,1]
	v_pk_fma_f32 v[36:37], v[2:3], v[46:47], v[34:35] op_sel_hi:[1,0,1]
	v_pk_fma_f32 v[34:35], v[0:1], v[46:47], v[40:41] op_sel_hi:[1,0,1]
	global_store_dwordx4 v[38:39], v[34:37], off offset:512 sc0 sc1
	v_pk_fma_f32 v[40:41], s[2:3], v[76:77], v[24:25] op_sel_hi:[0,1,1]
	v_pk_fma_f32 v[6:7], s[2:3], v[70:71], v[6:7] op_sel_hi:[0,1,1]
	v_pk_fma_f32 v[34:35], s[2:3], v[78:79], v[26:27] op_sel_hi:[0,1,1]
	v_pk_fma_f32 v[36:37], v[30:31], v[46:47], v[34:35] op_sel_hi:[1,0,1]
	v_pk_fma_f32 v[34:35], v[28:29], v[46:47], v[40:41] op_sel_hi:[1,0,1]
	global_store_dwordx4 v[38:39], v[34:37], off offset:576 sc0 sc1
	s_waitcnt lgkmcnt(0)
	v_pk_fma_f32 v[2:3], v[2:3], v[48:49], v[6:7] op_sel_hi:[1,0,1]
	v_pk_fma_f32 v[0:1], v[0:1], v[48:49], v[4:5] op_sel_hi:[1,0,1]
	v_lshl_add_u64 v[34:35], v[32:33], 0, s[0:1]
	s_mov_b32 s0, 0x160000
	v_pk_fma_f32 v[18:19], s[2:3], v[86:87], v[18:19] op_sel_hi:[0,1,1]
	v_pk_fma_f32 v[16:17], v[20:21], v[48:49], v[16:17] op_sel_hi:[1,0,1]
	v_add_co_u32_e32 v20, vcc, s0, v32
	v_pk_fma_f32 v[10:11], s[2:3], v[74:75], v[10:11] op_sel_hi:[0,1,1]
	v_pk_fma_f32 v[8:9], s[2:3], v[72:73], v[8:9] op_sel_hi:[0,1,1]
	global_store_dwordx4 v[34:35], v[0:3], off offset:512 sc0 sc1
	v_pk_fma_f32 v[4:5], s[2:3], v[64:65], v[24:25] op_sel_hi:[0,1,1]
	v_pk_fma_f32 v[18:19], v[22:23], v[48:49], v[18:19] op_sel_hi:[1,0,1]
	v_pk_fma_f32 v[0:1], s[2:3], v[66:67], v[26:27] op_sel_hi:[0,1,1]
	v_addc_co_u32_e32 v21, vcc, 0, v33, vcc
	v_pk_fma_f32 v[10:11], v[14:15], v[48:49], v[10:11] op_sel_hi:[1,0,1]
	v_pk_fma_f32 v[8:9], v[12:13], v[48:49], v[8:9] op_sel_hi:[1,0,1]
	v_pk_fma_f32 v[2:3], v[30:31], v[48:49], v[0:1] op_sel_hi:[1,0,1]
	v_pk_fma_f32 v[0:1], v[28:29], v[48:49], v[4:5] op_sel_hi:[1,0,1]
	global_store_dwordx4 v[20:21], v[16:19], off sc0 sc1
	global_store_dwordx4 v[34:35], v[8:11], off offset:64 sc0 sc1
	global_store_dwordx4 v[34:35], v[0:3], off offset:576 sc0 sc1
	s_waitcnt vmcnt(0)
	s_cbranch_scc0 .LBB5_36
	s_barrier
